# v28 + no grid barrier after the PLE projection GEMM + non-temporal stores for the layer 1-3 W_in bf16 copies written in P0
# speedup vs baseline: 1.0598x; 1.0006x over previous
.LBB0_157:
	s_or_b64 exec, exec, s[20:21]
	s_waitcnt vmcnt(0)
	ds_write2_b32 v10, v7, v11 offset1:66
	ds_write2_b32 v10, v13, v12 offset0:132 offset1:198
	v_add_u32_e32 v7, 0x400, v10
	ds_write2_b32 v7, v18, v17 offset0:8 offset1:74
	ds_write2_b32 v7, v20, v19 offset0:140 offset1:206
	v_add_u32_e32 v7, 0x800, v10
	ds_write2_b32 v7, v22, v21 offset0:16 offset1:82
	ds_write2_b32 v7, v24, v23 offset0:148 offset1:214
	v_add_u32_e32 v7, 0xc00, v10
	ds_write2_b32 v7, v26, v25 offset0:24 offset1:90
	ds_write2_b32 v7, v28, v27 offset0:156 offset1:222
	v_add_u32_e32 v7, 0x1000, v10
	s_mul_hi_i32 s4, s19, 0x1600000
	s_mul_i32 s19, s19, 0x1600000
	ds_write2_b32 v7, v30, v29 offset0:32 offset1:98
	ds_write2_b32 v7, v32, v31 offset0:164 offset1:230
	v_add_u32_e32 v7, 0x1400, v10
	s_add_u32 s17, s28, s19
	ds_write2_b32 v7, v34, v33 offset0:40 offset1:106
	ds_write2_b32 v7, v36, v35 offset0:172 offset1:238
	v_add_u32_e32 v7, 0x1800, v10
	s_addc_u32 s20, s29, s4
	ds_write2_b32 v7, v38, v37 offset0:48 offset1:114
	ds_write2_b32 v7, v40, v39 offset0:180 offset1:246
	v_add_u32_e32 v7, 0x1c00, v10
	s_ashr_i32 s19, s18, 31
	ds_write2_b32 v7, v42, v41 offset0:56 offset1:122
	ds_write2_b32 v7, v44, v43 offset0:188 offset1:254
	s_lshl_b64 s[4:5], s[18:19], 1
	s_waitcnt lgkmcnt(0)
	s_add_u32 s4, s17, s4
	v_add_u32_e32 v7, s16, v15
	s_addc_u32 s5, s20, s5
	v_add_u32_e32 v11, 0xffffe4f8, v7
	v_lshl_add_u64 v[8:9], s[4:5], 0, v[4:5]
	v_cmp_lt_u32_e32 vcc, s33, v11
	v_cmp_gt_i32_e64 s[4:5], s30, v7
	s_and_b64 s[16:17], s[4:5], vcc
	s_and_saveexec_b64 s[4:5], s[16:17]
	s_cbranch_execz .LBB0_159
	ds_read2_b32 v[12:13], v3 offset0:198 offset1:231
	ds_read2_b32 v[18:19], v3 offset0:132 offset1:165
	ds_read2_b32 v[22:23], v3 offset0:66 offset1:99
	ds_read2_b32 v[24:25], v3 offset1:33
	v_add_u32_e32 v11, 0xfffff000, v7
	v_cmp_gt_i32_e32 vcc, s34, v7
	s_waitcnt lgkmcnt(3)
	v_cvt_pk_bf16_f32 v21, v12, v13
	s_waitcnt lgkmcnt(2)
	v_cvt_pk_bf16_f32 v20, v18, v19
	v_cndmask_b32_e32 v12, v11, v7, vcc
	v_ashrrev_i32_e32 v13, 31, v12
	v_lshlrev_b64 v[12:13], 11, v[12:13]
	s_waitcnt lgkmcnt(1)
	v_cvt_pk_bf16_f32 v19, v22, v23
	s_waitcnt lgkmcnt(0)
	v_cvt_pk_bf16_f32 v18, v24, v25
	v_lshl_add_u64 v[12:13], v[8:9], 0, v[12:13]
	global_store_dwordx4 v[12:13], v[18:21], off nt
.LBB0_159:
	s_or_b64 exec, exec, s[4:5]
	v_add_u32_e32 v11, 8, v7
	v_add_u32_e32 v12, 0xffffe500, v7
	v_cmp_lt_u32_e32 vcc, s33, v12
	v_cmp_gt_i32_e64 s[4:5], s30, v11
	s_and_b64 s[16:17], s[4:5], vcc
	s_and_saveexec_b64 s[4:5], s[16:17]
	s_cbranch_execz .LBB0_161
	ds_read2_b32 v[12:13], v3 offset0:206 offset1:239
	ds_read2_b32 v[18:19], v3 offset0:140 offset1:173
	ds_read2_b32 v[22:23], v3 offset0:74 offset1:107
	ds_read2_b32 v[24:25], v3 offset0:8 offset1:41
	v_cmp_gt_i32_e32 vcc, s34, v11
	s_waitcnt lgkmcnt(3)
	v_cvt_pk_bf16_f32 v21, v12, v13
	v_add_u32_e32 v12, 0xfffff000, v11
	v_cndmask_b32_e32 v12, v12, v11, vcc
	v_ashrrev_i32_e32 v13, 31, v12
	v_lshlrev_b64 v[12:13], 11, v[12:13]
	s_waitcnt lgkmcnt(2)
	v_cvt_pk_bf16_f32 v20, v18, v19
	s_waitcnt lgkmcnt(1)
	v_cvt_pk_bf16_f32 v19, v22, v23
	s_waitcnt lgkmcnt(0)
	v_cvt_pk_bf16_f32 v18, v24, v25
	v_lshl_add_u64 v[12:13], v[8:9], 0, v[12:13]
	global_store_dwordx4 v[12:13], v[18:21], off nt
.LBB0_161:
	s_or_b64 exec, exec, s[4:5]
	v_add_u32_e32 v11, 16, v7
	v_add_u32_e32 v12, 0xffffe508, v7
	v_cmp_lt_u32_e32 vcc, s33, v12
	v_cmp_gt_i32_e64 s[4:5], s30, v11
	s_and_b64 s[16:17], s[4:5], vcc
	s_and_saveexec_b64 s[4:5], s[16:17]
	s_cbranch_execz .LBB0_163
	ds_read2_b32 v[12:13], v3 offset0:214 offset1:247
	ds_read2_b32 v[18:19], v3 offset0:148 offset1:181
	ds_read2_b32 v[22:23], v3 offset0:82 offset1:115
	ds_read2_b32 v[24:25], v3 offset0:16 offset1:49
	v_cmp_gt_i32_e32 vcc, s34, v11
	s_waitcnt lgkmcnt(3)
	v_cvt_pk_bf16_f32 v21, v12, v13
	v_add_u32_e32 v12, 0xfffff000, v11
	v_cndmask_b32_e32 v12, v12, v11, vcc
	v_ashrrev_i32_e32 v13, 31, v12
	v_lshlrev_b64 v[12:13], 11, v[12:13]
	s_waitcnt lgkmcnt(2)
	v_cvt_pk_bf16_f32 v20, v18, v19
	s_waitcnt lgkmcnt(1)
	v_cvt_pk_bf16_f32 v19, v22, v23
	s_waitcnt lgkmcnt(0)
	v_cvt_pk_bf16_f32 v18, v24, v25
	v_lshl_add_u64 v[12:13], v[8:9], 0, v[12:13]
	global_store_dwordx4 v[12:13], v[18:21], off nt
.LBB0_163:
	s_or_b64 exec, exec, s[4:5]
	v_add_u32_e32 v11, 24, v7
	v_add_u32_e32 v7, 0xffffe510, v7
	v_cmp_lt_u32_e32 vcc, s33, v7
	v_cmp_gt_i32_e64 s[4:5], s30, v11
	s_and_b64 s[16:17], s[4:5], vcc
	s_and_saveexec_b64 s[4:5], s[16:17]
	s_cbranch_execz .LBB0_90
	ds_read2_b32 v[12:13], v3 offset0:222 offset1:255
	ds_read2_b32 v[18:19], v3 offset0:156 offset1:189
	ds_read2_b32 v[22:23], v3 offset0:90 offset1:123
	ds_read2_b32 v[24:25], v3 offset0:24 offset1:57
	v_add_u32_e32 v7, 0xfffff000, v11
	v_cmp_gt_i32_e32 vcc, s34, v11
	s_waitcnt lgkmcnt(3)
	v_cvt_pk_bf16_f32 v21, v12, v13
	s_waitcnt lgkmcnt(2)
	v_cvt_pk_bf16_f32 v20, v18, v19
	v_cndmask_b32_e32 v12, v7, v11, vcc
	v_ashrrev_i32_e32 v13, 31, v12
	v_lshlrev_b64 v[12:13], 11, v[12:13]
	s_waitcnt lgkmcnt(1)
	v_cvt_pk_bf16_f32 v19, v22, v23
	s_waitcnt lgkmcnt(0)
	v_cvt_pk_bf16_f32 v18, v24, v25
	v_lshl_add_u64 v[8:9], v[8:9], 0, v[12:13]
	global_store_dwordx4 v[8:9], v[18:21], off nt
	s_branch .LBB0_90
